# gate|up GEMM epilogue (SwiGLU) re-emitted with packed f32 ops, same per-element operation order; accumulators cleared with 64-bit moves
# speedup vs baseline: 1.0091x; 1.0091x over previous
.LBB0_232:
	s_add_u32 s28, s84, s22
	s_addc_u32 s29, s85, s23
	s_and_b64 s[36:37], s[44:45], exec
	s_cselect_b32 s35, s29, s39
	s_cselect_b32 s46, s28, s38
	s_add_u32 s36, s86, s26
	s_addc_u32 s37, s87, s27
	s_and_b64 s[44:45], s[44:45], exec
	s_cselect_b32 s47, s37, s43
	s_cselect_b32 s48, s36, s42
	s_add_u32 s38, s38, 0x80080
	s_addc_u32 s39, s39, 0
	s_add_u32 s49, s42, 0x100
	v_mov_b32_e32 v2, 0
	s_addc_u32 s50, s43, 0
	s_mov_b32 s51, -2
	v_mov_b32_e32 v3, v2
	v_mov_b64_e32 v[4:5], 0
	v_mov_b64_e32 v[6:7], 0
	v_mov_b64_e32 v[8:9], 0
	v_mov_b64_e32 v[10:11], 0
	v_mov_b64_e32 v[12:13], 0
	v_mov_b64_e32 v[14:15], 0
	v_mov_b64_e32 v[16:17], 0
	v_mov_b64_e32 v[18:19], 0
	v_mov_b64_e32 v[20:21], 0
	v_mov_b64_e32 v[22:23], 0
	v_mov_b64_e32 v[24:25], 0
	v_mov_b64_e32 v[26:27], 0
	v_mov_b64_e32 v[28:29], 0
	v_mov_b64_e32 v[30:31], 0
	v_mov_b64_e32 v[32:33], 0
	v_mov_b64_e32 v[34:35], 0
	v_mov_b64_e32 v[36:37], 0
	v_mov_b64_e32 v[38:39], 0
	v_mov_b64_e32 v[40:41], 0
	v_mov_b64_e32 v[42:43], 0
	v_mov_b64_e32 v[44:45], 0
	v_mov_b64_e32 v[46:47], 0
	v_mov_b64_e32 v[48:49], 0
	v_mov_b64_e32 v[50:51], 0
	v_mov_b64_e32 v[52:53], 0
	v_mov_b64_e32 v[54:55], 0
	v_mov_b64_e32 v[56:57], 0
	v_mov_b64_e32 v[58:59], 0
	v_mov_b64_e32 v[60:61], 0
	v_mov_b64_e32 v[62:63], 0
	v_mov_b64_e32 v[64:65], 0
	v_mov_b64_e32 v[66:67], 0
	v_mov_b64_e32 v[68:69], 0
	v_mov_b64_e32 v[70:71], 0
	v_mov_b64_e32 v[72:73], 0
	v_mov_b64_e32 v[74:75], 0
	v_mov_b64_e32 v[76:77], 0
	v_mov_b64_e32 v[78:79], 0
	v_mov_b64_e32 v[80:81], 0
	v_mov_b64_e32 v[82:83], 0
	v_mov_b64_e32 v[84:85], 0
	v_mov_b64_e32 v[86:87], 0
	v_mov_b64_e32 v[88:89], 0
	v_mov_b64_e32 v[90:91], 0
	v_mov_b64_e32 v[92:93], 0
	v_mov_b64_e32 v[94:95], 0
	v_mov_b64_e32 v[96:97], 0
	v_mov_b64_e32 v[98:99], 0
	v_mov_b64_e32 v[100:101], 0
	v_mov_b64_e32 v[102:103], 0
	v_mov_b64_e32 v[104:105], 0
	v_mov_b64_e32 v[106:107], 0
	v_mov_b64_e32 v[108:109], 0
	v_mov_b64_e32 v[110:111], 0
	v_mov_b64_e32 v[112:113], 0
	v_mov_b64_e32 v[114:115], 0
	v_mov_b64_e32 v[116:117], 0
	v_mov_b64_e32 v[118:119], 0
	v_mov_b64_e32 v[120:121], 0
	v_mov_b64_e32 v[122:123], 0
	v_mov_b64_e32 v[124:125], 0
	v_mov_b64_e32 v[126:127], 0
	v_mov_b64_e32 v[128:129], 0

.LBB0_254:
	s_add_u32 s28, s84, s22
	s_addc_u32 s29, s85, s23
	s_and_b64 s[36:37], s[44:45], exec
	s_cselect_b32 s35, s29, s39
	s_cselect_b32 s46, s28, s38
	s_add_u32 s36, s86, s26
	s_addc_u32 s37, s87, s27
	s_and_b64 s[44:45], s[44:45], exec
	s_cselect_b32 s47, s37, s43
	s_cselect_b32 s48, s36, s42
	s_add_u32 s38, s38, 0x40080
	s_addc_u32 s39, s39, 0
	s_add_u32 s49, s42, 0x100
	v_mov_b32_e32 v34, 0
	s_addc_u32 s50, s43, 0
	s_mov_b32 s51, -2
	v_mov_b32_e32 v35, v34
	v_mov_b64_e32 v[36:37], 0
	v_mov_b64_e32 v[38:39], 0
	v_mov_b64_e32 v[40:41], 0
	v_mov_b64_e32 v[42:43], 0
	v_mov_b64_e32 v[44:45], 0
	v_mov_b64_e32 v[46:47], 0
	v_mov_b64_e32 v[48:49], 0
	v_mov_b64_e32 v[50:51], 0
	v_mov_b64_e32 v[52:53], 0
	v_mov_b64_e32 v[54:55], 0
	v_mov_b64_e32 v[56:57], 0
	v_mov_b64_e32 v[58:59], 0
	v_mov_b64_e32 v[60:61], 0
	v_mov_b64_e32 v[62:63], 0
	v_mov_b64_e32 v[64:65], 0
	v_mov_b64_e32 v[66:67], 0
	v_mov_b64_e32 v[68:69], 0
	v_mov_b64_e32 v[70:71], 0
	v_mov_b64_e32 v[72:73], 0
	v_mov_b64_e32 v[74:75], 0
	v_mov_b64_e32 v[76:77], 0
	v_mov_b64_e32 v[78:79], 0
	v_mov_b64_e32 v[80:81], 0
	v_mov_b64_e32 v[82:83], 0
	v_mov_b64_e32 v[84:85], 0
	v_mov_b64_e32 v[86:87], 0
	v_mov_b64_e32 v[88:89], 0
	v_mov_b64_e32 v[90:91], 0
	v_mov_b64_e32 v[92:93], 0
	v_mov_b64_e32 v[94:95], 0
	v_mov_b64_e32 v[96:97], 0
	v_mov_b64_e32 v[98:99], 0
	v_mov_b64_e32 v[100:101], 0
	v_mov_b64_e32 v[102:103], 0
	v_mov_b64_e32 v[104:105], 0
	v_mov_b64_e32 v[106:107], 0
	v_mov_b64_e32 v[108:109], 0
	v_mov_b64_e32 v[110:111], 0
	v_mov_b64_e32 v[112:113], 0
	v_mov_b64_e32 v[114:115], 0
	v_mov_b64_e32 v[116:117], 0
	v_mov_b64_e32 v[118:119], 0
	v_mov_b64_e32 v[120:121], 0
	v_mov_b64_e32 v[122:123], 0
	v_mov_b64_e32 v[124:125], 0
	v_mov_b64_e32 v[126:127], 0
	v_mov_b64_e32 v[128:129], 0
	v_mov_b64_e32 v[130:131], 0
	v_mov_b64_e32 v[132:133], 0
	v_mov_b64_e32 v[134:135], 0
	v_mov_b64_e32 v[136:137], 0
	v_mov_b64_e32 v[138:139], 0
	v_mov_b64_e32 v[140:141], 0
	v_mov_b64_e32 v[142:143], 0
	v_mov_b64_e32 v[144:145], 0
	v_mov_b64_e32 v[146:147], 0
	v_mov_b64_e32 v[148:149], 0
	v_mov_b64_e32 v[150:151], 0
	v_mov_b64_e32 v[152:153], 0
	v_mov_b64_e32 v[154:155], 0
	v_mov_b64_e32 v[156:157], 0
	v_mov_b64_e32 v[158:159], 0
	v_mov_b64_e32 v[160:161], 0

.LBB0_311:
	s_add_u32 s38, s84, s6
	s_addc_u32 s39, s85, s7
	s_and_b64 s[40:41], s[8:9], exec
	s_cselect_b32 s49, s39, s43
	s_cselect_b32 s50, s38, s42
	s_add_u32 s40, s86, s26
	s_addc_u32 s41, s87, s27
	s_and_b64 s[8:9], s[8:9], exec
	s_cselect_b32 s8, s41, s45
	s_cselect_b32 s9, s40, s44
	s_add_u32 s42, s42, 0x80080
	s_addc_u32 s43, s43, 0
	s_add_u32 s51, s44, 0x100
	v_mov_b32_e32 v2, 0
	s_addc_u32 s52, s45, 0
	s_mov_b32 s53, -2
	v_mov_b32_e32 v3, v2
	v_mov_b64_e32 v[4:5], 0
	v_mov_b64_e32 v[6:7], 0
	v_mov_b64_e32 v[8:9], 0
	v_mov_b64_e32 v[10:11], 0
	v_mov_b64_e32 v[12:13], 0
	v_mov_b64_e32 v[14:15], 0
	v_mov_b64_e32 v[16:17], 0
	v_mov_b64_e32 v[18:19], 0
	v_mov_b64_e32 v[20:21], 0
	v_mov_b64_e32 v[22:23], 0
	v_mov_b64_e32 v[24:25], 0
	v_mov_b64_e32 v[26:27], 0
	v_mov_b64_e32 v[28:29], 0
	v_mov_b64_e32 v[30:31], 0
	v_mov_b64_e32 v[32:33], 0
	v_mov_b64_e32 v[34:35], 0
	v_mov_b64_e32 v[36:37], 0
	v_mov_b64_e32 v[38:39], 0
	v_mov_b64_e32 v[40:41], 0
	v_mov_b64_e32 v[42:43], 0
	v_mov_b64_e32 v[44:45], 0
	v_mov_b64_e32 v[46:47], 0
	v_mov_b64_e32 v[48:49], 0
	v_mov_b64_e32 v[50:51], 0
	v_mov_b64_e32 v[52:53], 0
	v_mov_b64_e32 v[54:55], 0
	v_mov_b64_e32 v[56:57], 0
	v_mov_b64_e32 v[58:59], 0
	v_mov_b64_e32 v[60:61], 0
	v_mov_b64_e32 v[62:63], 0
	v_mov_b64_e32 v[64:65], 0
	v_mov_b64_e32 v[66:67], 0
	v_mov_b64_e32 v[68:69], 0
	v_mov_b64_e32 v[70:71], 0
	v_mov_b64_e32 v[72:73], 0
	v_mov_b64_e32 v[74:75], 0
	v_mov_b64_e32 v[76:77], 0
	v_mov_b64_e32 v[78:79], 0
	v_mov_b64_e32 v[80:81], 0
	v_mov_b64_e32 v[82:83], 0
	v_mov_b64_e32 v[84:85], 0
	v_mov_b64_e32 v[86:87], 0
	v_mov_b64_e32 v[88:89], 0
	v_mov_b64_e32 v[90:91], 0
	v_mov_b64_e32 v[92:93], 0
	v_mov_b64_e32 v[94:95], 0
	v_mov_b64_e32 v[96:97], 0
	v_mov_b64_e32 v[98:99], 0
	v_mov_b64_e32 v[100:101], 0
	v_mov_b64_e32 v[102:103], 0
	v_mov_b64_e32 v[104:105], 0
	v_mov_b64_e32 v[106:107], 0
	v_mov_b64_e32 v[108:109], 0
	v_mov_b64_e32 v[110:111], 0
	v_mov_b64_e32 v[112:113], 0
	v_mov_b64_e32 v[114:115], 0
	v_mov_b64_e32 v[116:117], 0
	v_mov_b64_e32 v[118:119], 0
	v_mov_b64_e32 v[120:121], 0
	v_mov_b64_e32 v[122:123], 0
	v_mov_b64_e32 v[124:125], 0
	v_mov_b64_e32 v[126:127], 0
	v_mov_b64_e32 v[128:129], 0

.LBB0_434:
	v_lshrrev_b32_e32 v18, 1, v14
	v_and_b32_e32 v17, 15, v14
	v_and_b32_e32 v140, 24, v18
	s_lshl_b32 s13, s13, 5
	v_lshl_or_b32 v1, s10, 6, v17
	v_lshlrev_b32_e32 v18, 1, v140
	v_lshlrev_b32_e32 v14, 2, v14
	s_lshl_b32 s14, s10, 13
	s_and_b32 s10, s13, 0x60
	v_lshl_or_b32 v17, v17, 6, v18
	v_and_b32_e32 v14, 32, v14
	s_lshl_b32 s13, s10, 7
	s_add_i32 m0, s4, 0x18000
	v_lshl_add_u64 v[8:9], v[8:9], 0, s[30:31]
	v_bitop3_b32 v141, v17, s13, v14 bitop3:0xde
	v_bitop3_b32 v14, v17, s14, v14 bitop3:0xde
	s_waitcnt vmcnt(4)
	s_barrier
	global_load_lds_dwordx4 v[8:9], off
	v_lshl_add_u64 v[6:7], v[6:7], 0, s[30:31]
	s_add_i32 m0, s4, 0x1a000
	s_add_i32 s13, s4, 0x8000
	s_add_i32 s14, s4, 0xa000
	global_load_lds_dwordx4 v[6:7], off
	v_lshl_add_u64 v[4:5], v[4:5], 0, s[30:31]
	s_mov_b32 m0, s13
	s_add_u32 s16, s36, 0x80080
	global_load_lds_dwordx4 v[4:5], off
	v_lshl_add_u64 v[2:3], v[2:3], 0, s[30:31]
	s_mov_b32 m0, s14
	s_addc_u32 s17, s37, 0
	global_load_lds_dwordx4 v[2:3], off
	s_add_i32 m0, s4, 0x1c000
	v_lshl_add_u64 v[2:3], s[16:17], 0, v[194:195]
	global_load_lds_dwordx4 v[2:3], off
	v_lshl_add_u64 v[2:3], s[16:17], 0, v[134:135]
	s_add_i32 m0, s4, 0x1e000
	s_add_u32 s16, s22, s26
	global_load_lds_dwordx4 v[2:3], off
	v_lshlrev_b32_e32 v2, 15, v10
	v_and_b32_e32 v2, 0xffff0000, v2
	s_addc_u32 s17, s23, s27
	v_lshl_add_u32 v2, v11, 12, v2
	v_and_b32_e32 v3, 1, v10
	v_lshl_or_b32 v2, v3, 6, v2
	s_add_u32 s18, s57, s26
	v_lshl_add_u32 v2, v12, 1, v2
	v_mov_b32_e32 v3, v195
	s_addc_u32 s19, s58, s27
	v_lshl_add_u64 v[136:137], s[18:19], 0, v[2:3]
	v_lshlrev_b32_e32 v2, 15, v13
	v_and_b32_e32 v2, 0xffff0000, v2
	v_lshl_add_u32 v2, v15, 12, v2
	v_and_b32_e32 v3, 1, v13
	v_lshl_or_b32 v2, v3, 6, v2
	s_waitcnt vmcnt(6)
	v_lshl_add_u32 v2, v16, 1, v2
	v_mov_b32_e32 v3, v195
	v_lshl_add_u64 v[138:139], s[18:19], 0, v[2:3]
	s_add_u32 s18, s59, s6
	v_mov_b32_e32 v2, 0
	s_addc_u32 s19, s60, s7
	s_mov_b32 s24, -2
	s_mov_b64 s[44:45], 0
	v_add_u32_e32 v142, 0, v14
	v_mov_b32_e32 v3, v2
	v_mov_b64_e32 v[4:5], 0
	v_mov_b64_e32 v[6:7], 0
	v_mov_b64_e32 v[8:9], 0
	v_mov_b64_e32 v[10:11], 0
	v_mov_b64_e32 v[12:13], 0
	v_mov_b64_e32 v[14:15], 0
	v_mov_b64_e32 v[16:17], 0
	v_mov_b64_e32 v[18:19], 0
	v_mov_b64_e32 v[20:21], 0
	v_mov_b64_e32 v[22:23], 0
	v_mov_b64_e32 v[24:25], 0
	v_mov_b64_e32 v[26:27], 0
	v_mov_b64_e32 v[28:29], 0
	v_mov_b64_e32 v[30:31], 0
	v_mov_b64_e32 v[32:33], 0
	v_mov_b64_e32 v[34:35], 0
	v_mov_b64_e32 v[36:37], 0
	v_mov_b64_e32 v[38:39], 0
	v_mov_b64_e32 v[40:41], 0
	v_mov_b64_e32 v[42:43], 0
	v_mov_b64_e32 v[44:45], 0
	v_mov_b64_e32 v[46:47], 0
	v_mov_b64_e32 v[48:49], 0
	v_mov_b64_e32 v[50:51], 0
	v_mov_b64_e32 v[52:53], 0
	v_mov_b64_e32 v[54:55], 0
	v_mov_b64_e32 v[56:57], 0
	v_mov_b64_e32 v[58:59], 0
	v_mov_b64_e32 v[60:61], 0
	v_mov_b64_e32 v[62:63], 0
	v_mov_b64_e32 v[64:65], 0
	v_mov_b64_e32 v[66:67], 0
	v_mov_b64_e32 v[68:69], 0
	v_mov_b64_e32 v[70:71], 0
	v_mov_b64_e32 v[72:73], 0
	v_mov_b64_e32 v[74:75], 0
	v_mov_b64_e32 v[76:77], 0
	v_mov_b64_e32 v[78:79], 0
	v_mov_b64_e32 v[80:81], 0
	v_mov_b64_e32 v[82:83], 0
	v_mov_b64_e32 v[84:85], 0
	v_mov_b64_e32 v[86:87], 0
	v_mov_b64_e32 v[88:89], 0
	v_mov_b64_e32 v[90:91], 0
	v_mov_b64_e32 v[92:93], 0
	v_mov_b64_e32 v[94:95], 0
	v_mov_b64_e32 v[96:97], 0
	v_mov_b64_e32 v[98:99], 0
	v_mov_b64_e32 v[100:101], 0
	v_mov_b64_e32 v[102:103], 0
	v_mov_b64_e32 v[104:105], 0
	v_mov_b64_e32 v[106:107], 0
	v_mov_b64_e32 v[108:109], 0
	v_mov_b64_e32 v[110:111], 0
	v_mov_b64_e32 v[112:113], 0
	v_mov_b64_e32 v[114:115], 0
	v_mov_b64_e32 v[116:117], 0
	v_mov_b64_e32 v[118:119], 0
	v_mov_b64_e32 v[120:121], 0
	v_mov_b64_e32 v[122:123], 0
	v_mov_b64_e32 v[124:125], 0
	v_mov_b64_e32 v[126:127], 0
	v_mov_b64_e32 v[128:129], 0
	s_barrier

.LBB0_442:
	v_lshrrev_b32_e32 v18, 1, v14
	v_and_b32_e32 v17, 15, v14
	v_and_b32_e32 v182, 24, v18
	s_lshl_b32 s13, s13, 5
	v_lshl_or_b32 v181, s10, 6, v17
	v_lshlrev_b32_e32 v18, 1, v182
	v_lshlrev_b32_e32 v14, 2, v14
	s_lshl_b32 s14, s10, 13
	s_and_b32 s10, s13, 0x60
	v_lshl_or_b32 v17, v17, 6, v18
	v_and_b32_e32 v14, 32, v14
	s_lshl_b32 s13, s10, 7
	s_add_i32 m0, s4, 0x18000
	v_lshl_add_u64 v[8:9], v[8:9], 0, s[30:31]
	v_bitop3_b32 v183, v17, s13, v14 bitop3:0xde
	v_bitop3_b32 v14, v17, s14, v14 bitop3:0xde
	s_waitcnt vmcnt(4)
	s_barrier
	global_load_lds_dwordx4 v[8:9], off
	v_lshl_add_u64 v[6:7], v[6:7], 0, s[30:31]
	s_add_i32 m0, s4, 0x1a000
	s_add_i32 s13, s4, 0x8000
	s_add_i32 s14, s4, 0xa000
	global_load_lds_dwordx4 v[6:7], off
	v_lshl_add_u64 v[4:5], v[4:5], 0, s[30:31]
	s_mov_b32 m0, s13
	s_add_u32 s16, s36, 0x40080
	global_load_lds_dwordx4 v[4:5], off
	v_lshl_add_u64 v[2:3], v[2:3], 0, s[30:31]
	s_mov_b32 m0, s14
	s_addc_u32 s17, s37, 0
	global_load_lds_dwordx4 v[2:3], off
	s_add_i32 m0, s4, 0x1c000
	v_lshl_add_u64 v[2:3], s[16:17], 0, v[194:195]
	global_load_lds_dwordx4 v[2:3], off
	v_lshl_add_u64 v[2:3], s[16:17], 0, v[166:167]
	s_add_i32 m0, s4, 0x1e000
	s_add_u32 s16, s22, s26
	global_load_lds_dwordx4 v[2:3], off
	v_lshlrev_b32_e32 v2, 14, v10
	v_and_b32_e32 v2, 0xffff8000, v2
	s_addc_u32 s17, s23, s27
	v_lshl_add_u32 v2, v11, 11, v2
	v_and_b32_e32 v3, 1, v10
	v_lshl_or_b32 v2, v3, 6, v2
	s_add_u32 s18, s61, s26
	v_lshl_add_u32 v2, v12, 1, v2
	v_mov_b32_e32 v3, v195
	s_addc_u32 s19, s62, s27
	v_lshl_add_u64 v[168:169], s[18:19], 0, v[2:3]
	v_lshlrev_b32_e32 v2, 14, v13
	v_and_b32_e32 v2, 0xffff8000, v2
	v_lshl_add_u32 v2, v15, 11, v2
	v_and_b32_e32 v3, 1, v13
	v_lshl_or_b32 v2, v3, 6, v2
	s_waitcnt vmcnt(6)
	v_lshl_add_u32 v2, v16, 1, v2
	v_mov_b32_e32 v3, v195
	v_lshl_add_u64 v[170:171], s[18:19], 0, v[2:3]
	s_add_u32 s18, s59, s6
	v_mov_b32_e32 v34, 0
	s_addc_u32 s19, s60, s7
	s_mov_b32 s24, -2
	s_mov_b64 s[6:7], 0
	v_add_u32_e32 v184, 0, v14
	v_mov_b32_e32 v35, v34
	v_mov_b64_e32 v[36:37], 0
	v_mov_b64_e32 v[38:39], 0
	v_mov_b64_e32 v[40:41], 0
	v_mov_b64_e32 v[42:43], 0
	v_mov_b64_e32 v[44:45], 0
	v_mov_b64_e32 v[46:47], 0
	v_mov_b64_e32 v[48:49], 0
	v_mov_b64_e32 v[50:51], 0
	v_mov_b64_e32 v[52:53], 0
	v_mov_b64_e32 v[54:55], 0
	v_mov_b64_e32 v[56:57], 0
	v_mov_b64_e32 v[58:59], 0
	v_mov_b64_e32 v[60:61], 0
	v_mov_b64_e32 v[62:63], 0
	v_mov_b64_e32 v[64:65], 0
	v_mov_b64_e32 v[66:67], 0
	v_mov_b64_e32 v[68:69], 0
	v_mov_b64_e32 v[70:71], 0
	v_mov_b64_e32 v[72:73], 0
	v_mov_b64_e32 v[74:75], 0
	v_mov_b64_e32 v[76:77], 0
	v_mov_b64_e32 v[78:79], 0
	v_mov_b64_e32 v[80:81], 0
	v_mov_b64_e32 v[82:83], 0
	v_mov_b64_e32 v[84:85], 0
	v_mov_b64_e32 v[86:87], 0
	v_mov_b64_e32 v[88:89], 0
	v_mov_b64_e32 v[90:91], 0
	v_mov_b64_e32 v[92:93], 0
	v_mov_b64_e32 v[94:95], 0
	v_mov_b64_e32 v[96:97], 0
	v_mov_b64_e32 v[98:99], 0
	v_mov_b64_e32 v[100:101], 0
	v_mov_b64_e32 v[102:103], 0
	v_mov_b64_e32 v[104:105], 0
	v_mov_b64_e32 v[106:107], 0
	v_mov_b64_e32 v[108:109], 0
	v_mov_b64_e32 v[110:111], 0
	v_mov_b64_e32 v[112:113], 0
	v_mov_b64_e32 v[114:115], 0
	v_mov_b64_e32 v[116:117], 0
	v_mov_b64_e32 v[118:119], 0
	v_mov_b64_e32 v[120:121], 0
	v_mov_b64_e32 v[122:123], 0
	v_mov_b64_e32 v[124:125], 0
	v_mov_b64_e32 v[126:127], 0
	v_mov_b64_e32 v[128:129], 0
	v_mov_b64_e32 v[130:131], 0
	v_mov_b64_e32 v[132:133], 0
	v_mov_b64_e32 v[134:135], 0
	v_mov_b64_e32 v[136:137], 0
	v_mov_b64_e32 v[138:139], 0
	v_mov_b64_e32 v[140:141], 0
	v_mov_b64_e32 v[142:143], 0
	v_mov_b64_e32 v[144:145], 0
	v_mov_b64_e32 v[146:147], 0
	v_mov_b64_e32 v[148:149], 0
	v_mov_b64_e32 v[150:151], 0
	v_mov_b64_e32 v[152:153], 0
	v_mov_b64_e32 v[154:155], 0
	v_mov_b64_e32 v[156:157], 0
	v_mov_b64_e32 v[158:159], 0
	v_mov_b64_e32 v[160:161], 0
	s_barrier

.LBB0_682:
	s_add_u32 s28, s2, s22
	s_addc_u32 s29, s44, s23
	s_and_b64 s[36:37], s[42:43], exec
	s_cselect_b32 s47, s29, s39
	s_cselect_b32 s48, s28, s38
	s_add_u32 s36, s45, s26
	s_addc_u32 s37, s46, s27
	s_and_b64 s[42:43], s[42:43], exec
	s_cselect_b32 s49, s37, s41
	s_cselect_b32 s50, s36, s40
	s_add_u32 s38, s38, 0x80080
	s_addc_u32 s39, s39, 0
	s_add_u32 s51, s40, 0x100
	v_mov_b32_e32 v2, 0
	s_addc_u32 s52, s41, 0
	s_mov_b32 s53, -2
	v_mov_b32_e32 v3, v2
	v_mov_b64_e32 v[4:5], 0
	v_mov_b64_e32 v[6:7], 0
	v_mov_b64_e32 v[8:9], 0
	v_mov_b64_e32 v[10:11], 0
	v_mov_b64_e32 v[12:13], 0
	v_mov_b64_e32 v[14:15], 0
	v_mov_b64_e32 v[16:17], 0
	v_mov_b64_e32 v[18:19], 0
	v_mov_b64_e32 v[20:21], 0
	v_mov_b64_e32 v[22:23], 0
	v_mov_b64_e32 v[24:25], 0
	v_mov_b64_e32 v[26:27], 0
	v_mov_b64_e32 v[28:29], 0
	v_mov_b64_e32 v[30:31], 0
	v_mov_b64_e32 v[32:33], 0
	v_mov_b64_e32 v[34:35], 0
	v_mov_b64_e32 v[36:37], 0
	v_mov_b64_e32 v[38:39], 0
	v_mov_b64_e32 v[40:41], 0
	v_mov_b64_e32 v[42:43], 0
	v_mov_b64_e32 v[44:45], 0
	v_mov_b64_e32 v[46:47], 0
	v_mov_b64_e32 v[48:49], 0
	v_mov_b64_e32 v[50:51], 0
	v_mov_b64_e32 v[52:53], 0
	v_mov_b64_e32 v[54:55], 0
	v_mov_b64_e32 v[56:57], 0
	v_mov_b64_e32 v[58:59], 0
	v_mov_b64_e32 v[60:61], 0
	v_mov_b64_e32 v[62:63], 0
	v_mov_b64_e32 v[64:65], 0
	v_mov_b64_e32 v[66:67], 0
	v_mov_b64_e32 v[68:69], 0
	v_mov_b64_e32 v[70:71], 0
	v_mov_b64_e32 v[72:73], 0
	v_mov_b64_e32 v[74:75], 0
	v_mov_b64_e32 v[76:77], 0
	v_mov_b64_e32 v[78:79], 0
	v_mov_b64_e32 v[80:81], 0
	v_mov_b64_e32 v[82:83], 0
	v_mov_b64_e32 v[84:85], 0
	v_mov_b64_e32 v[86:87], 0
	v_mov_b64_e32 v[88:89], 0
	v_mov_b64_e32 v[90:91], 0
	v_mov_b64_e32 v[92:93], 0
	v_mov_b64_e32 v[94:95], 0
	v_mov_b64_e32 v[96:97], 0
	v_mov_b64_e32 v[98:99], 0
	v_mov_b64_e32 v[100:101], 0
	v_mov_b64_e32 v[102:103], 0
	v_mov_b64_e32 v[104:105], 0
	v_mov_b64_e32 v[106:107], 0
	v_mov_b64_e32 v[108:109], 0
	v_mov_b64_e32 v[110:111], 0
	v_mov_b64_e32 v[112:113], 0
	v_mov_b64_e32 v[114:115], 0
	v_mov_b64_e32 v[116:117], 0
	v_mov_b64_e32 v[118:119], 0
	v_mov_b64_e32 v[120:121], 0
	v_mov_b64_e32 v[122:123], 0
	v_mov_b64_e32 v[124:125], 0
	v_mov_b64_e32 v[126:127], 0
	v_mov_b64_e32 v[128:129], 0

.LBB0_704:
	s_add_u32 s28, s2, s22
	s_addc_u32 s29, s44, s23
	s_and_b64 s[36:37], s[42:43], exec
	s_cselect_b32 s47, s29, s39
	s_cselect_b32 s48, s28, s38
	s_add_u32 s36, s45, s26
	s_addc_u32 s37, s46, s27
	s_and_b64 s[42:43], s[42:43], exec
	s_cselect_b32 s49, s37, s41
	s_cselect_b32 s50, s36, s40
	s_add_u32 s38, s38, 0x40080
	s_addc_u32 s39, s39, 0
	s_add_u32 s51, s40, 0x100
	v_mov_b32_e32 v34, 0
	s_addc_u32 s52, s41, 0
	s_mov_b32 s53, -2
	v_mov_b32_e32 v35, v34
	v_mov_b64_e32 v[36:37], 0
	v_mov_b64_e32 v[38:39], 0
	v_mov_b64_e32 v[40:41], 0
	v_mov_b64_e32 v[42:43], 0
	v_mov_b64_e32 v[44:45], 0
	v_mov_b64_e32 v[46:47], 0
	v_mov_b64_e32 v[48:49], 0
	v_mov_b64_e32 v[50:51], 0
	v_mov_b64_e32 v[52:53], 0
	v_mov_b64_e32 v[54:55], 0
	v_mov_b64_e32 v[56:57], 0
	v_mov_b64_e32 v[58:59], 0
	v_mov_b64_e32 v[60:61], 0
	v_mov_b64_e32 v[62:63], 0
	v_mov_b64_e32 v[64:65], 0
	v_mov_b64_e32 v[66:67], 0
	v_mov_b64_e32 v[68:69], 0
	v_mov_b64_e32 v[70:71], 0
	v_mov_b64_e32 v[72:73], 0
	v_mov_b64_e32 v[74:75], 0
	v_mov_b64_e32 v[76:77], 0
	v_mov_b64_e32 v[78:79], 0
	v_mov_b64_e32 v[80:81], 0
	v_mov_b64_e32 v[82:83], 0
	v_mov_b64_e32 v[84:85], 0
	v_mov_b64_e32 v[86:87], 0
	v_mov_b64_e32 v[88:89], 0
	v_mov_b64_e32 v[90:91], 0
	v_mov_b64_e32 v[92:93], 0
	v_mov_b64_e32 v[94:95], 0
	v_mov_b64_e32 v[96:97], 0
	v_mov_b64_e32 v[98:99], 0
	v_mov_b64_e32 v[100:101], 0
	v_mov_b64_e32 v[102:103], 0
	v_mov_b64_e32 v[104:105], 0
	v_mov_b64_e32 v[106:107], 0
	v_mov_b64_e32 v[108:109], 0
	v_mov_b64_e32 v[110:111], 0
	v_mov_b64_e32 v[112:113], 0
	v_mov_b64_e32 v[114:115], 0
	v_mov_b64_e32 v[116:117], 0
	v_mov_b64_e32 v[118:119], 0
	v_mov_b64_e32 v[120:121], 0
	v_mov_b64_e32 v[122:123], 0
	v_mov_b64_e32 v[124:125], 0
	v_mov_b64_e32 v[126:127], 0
	v_mov_b64_e32 v[128:129], 0
	v_mov_b64_e32 v[130:131], 0
	v_mov_b64_e32 v[132:133], 0
	v_mov_b64_e32 v[134:135], 0
	v_mov_b64_e32 v[136:137], 0
	v_mov_b64_e32 v[138:139], 0
	v_mov_b64_e32 v[140:141], 0
	v_mov_b64_e32 v[142:143], 0
	v_mov_b64_e32 v[144:145], 0
	v_mov_b64_e32 v[146:147], 0
	v_mov_b64_e32 v[148:149], 0
	v_mov_b64_e32 v[150:151], 0
	v_mov_b64_e32 v[152:153], 0
	v_mov_b64_e32 v[154:155], 0
	v_mov_b64_e32 v[156:157], 0
	v_mov_b64_e32 v[158:159], 0
	v_mov_b64_e32 v[160:161], 0

.LBB0_996:
	s_nop 15
	s_nop 15
	s_ashr_i32 s6, s13, 1
	v_add_u32_e32 v8, s10, v233
	v_add_u32_e32 v2, s6, v235
	v_mov_b64_e32 v[4:5], s[22:23]
	s_movk_i32 s8, 0x600
	v_ashrrev_i32_e32 v3, 31, v2
	s_and_b64 vcc, exec, s[58:59]
	s_mov_b32 s13, s73
	s_mov_b32 s10, s44
	s_mov_b64 s[26:27], s[56:57]
	s_mov_b32 s100, 0xbfb8aa3b
	s_mov_b32 s101, 0x41000000
	v_mad_i64_i32 v[6:7], s[6:7], v8, s8, v[4:5]
	v_add_u32_e32 v9, 16, v8
	v_mad_i64_i32 v[46:47], s[6:7], v9, s8, v[4:5]
	v_pk_mul_f32 v[18:19], v[190:191], s[100:101] op_sel_hi:[1,0]
	v_pk_mul_f32 v[20:21], v[192:193], s[100:101] op_sel_hi:[1,0]
	v_pk_mul_f32 v[22:23], v[182:183], s[100:101] op_sel_hi:[1,0]
	v_pk_mul_f32 v[24:25], v[184:185], s[100:101] op_sel_hi:[1,0]
	v_pk_mul_f32 v[26:27], v[174:175], s[100:101] op_sel_hi:[1,0]
	v_pk_mul_f32 v[28:29], v[176:177], s[100:101] op_sel_hi:[1,0]
	v_pk_mul_f32 v[30:31], v[166:167], s[100:101] op_sel_hi:[1,0]
	v_pk_mul_f32 v[32:33], v[168:169], s[100:101] op_sel_hi:[1,0]
	v_lshl_add_u64 v[6:7], v[6:7], 0, v[2:3]
	v_lshl_add_u64 v[46:47], v[46:47], 0, v[2:3]
	v_exp_f32_e32 v18, v18
	v_exp_f32_e32 v19, v19
	v_exp_f32_e32 v20, v20
	v_exp_f32_e32 v21, v21
	v_exp_f32_e32 v22, v22
	v_exp_f32_e32 v23, v23
	v_exp_f32_e32 v24, v24
	v_exp_f32_e32 v25, v25
	v_exp_f32_e32 v26, v26
	v_exp_f32_e32 v27, v27
	v_exp_f32_e32 v28, v28
	v_exp_f32_e32 v29, v29
	v_exp_f32_e32 v30, v30
	v_exp_f32_e32 v31, v31
	v_exp_f32_e32 v32, v32
	v_exp_f32_e32 v33, v33
	v_pk_add_f32 v[18:19], v[18:19], 1.0 op_sel_hi:[1,0]
	v_pk_add_f32 v[20:21], v[20:21], 1.0 op_sel_hi:[1,0]
	v_pk_add_f32 v[22:23], v[22:23], 1.0 op_sel_hi:[1,0]
	v_pk_add_f32 v[24:25], v[24:25], 1.0 op_sel_hi:[1,0]
	v_pk_add_f32 v[26:27], v[26:27], 1.0 op_sel_hi:[1,0]
	v_pk_add_f32 v[28:29], v[28:29], 1.0 op_sel_hi:[1,0]
	v_pk_add_f32 v[30:31], v[30:31], 1.0 op_sel_hi:[1,0]
	v_pk_add_f32 v[32:33], v[32:33], 1.0 op_sel_hi:[1,0]
	v_rcp_f32_e32 v18, v18
	v_rcp_f32_e32 v19, v19
	v_rcp_f32_e32 v20, v20
	v_rcp_f32_e32 v21, v21
	v_rcp_f32_e32 v22, v22
	v_rcp_f32_e32 v23, v23
	v_rcp_f32_e32 v24, v24
	v_rcp_f32_e32 v25, v25
	v_rcp_f32_e32 v26, v26
	v_rcp_f32_e32 v27, v27
	v_rcp_f32_e32 v28, v28
	v_rcp_f32_e32 v29, v29
	v_rcp_f32_e32 v30, v30
	v_rcp_f32_e32 v31, v31
	v_rcp_f32_e32 v32, v32
	v_rcp_f32_e32 v33, v33
	v_pk_mul_f32 v[18:19], v[190:191], v[18:19]
	v_pk_mul_f32 v[20:21], v[192:193], v[20:21]
	v_pk_mul_f32 v[22:23], v[182:183], v[22:23]
	v_pk_mul_f32 v[24:25], v[184:185], v[24:25]
	v_pk_mul_f32 v[26:27], v[174:175], v[26:27]
	v_pk_mul_f32 v[28:29], v[176:177], v[28:29]
	v_pk_mul_f32 v[30:31], v[166:167], v[30:31]
	v_pk_mul_f32 v[32:33], v[168:169], v[32:33]
	v_pk_mul_f32 v[18:19], v[18:19], v[186:187]
	v_pk_mul_f32 v[20:21], v[20:21], v[188:189]
	v_pk_mul_f32 v[22:23], v[22:23], v[178:179]
	v_pk_mul_f32 v[24:25], v[24:25], v[180:181]
	v_pk_mul_f32 v[26:27], v[26:27], v[170:171]
	v_pk_mul_f32 v[28:29], v[28:29], v[172:173]
	v_pk_mul_f32 v[30:31], v[30:31], v[162:163]
	v_pk_mul_f32 v[32:33], v[32:33], v[164:165]
	v_pk_mul_f32 v[18:19], v[18:19], s[100:101] op_sel:[0,1] op_sel_hi:[1,1]
	v_pk_mul_f32 v[20:21], v[20:21], s[100:101] op_sel:[0,1] op_sel_hi:[1,1]
	v_pk_mul_f32 v[22:23], v[22:23], s[100:101] op_sel:[0,1] op_sel_hi:[1,1]
	v_pk_mul_f32 v[24:25], v[24:25], s[100:101] op_sel:[0,1] op_sel_hi:[1,1]
	v_pk_mul_f32 v[26:27], v[26:27], s[100:101] op_sel:[0,1] op_sel_hi:[1,1]
	v_pk_mul_f32 v[28:29], v[28:29], s[100:101] op_sel:[0,1] op_sel_hi:[1,1]
	v_pk_mul_f32 v[30:31], v[30:31], s[100:101] op_sel:[0,1] op_sel_hi:[1,1]
	v_pk_mul_f32 v[32:33], v[32:33], s[100:101] op_sel:[0,1] op_sel_hi:[1,1]
	v_cvt_pk_fp8_f32 v10, v18, v19
	v_cvt_pk_fp8_f32 v12, v26, v27
	v_cvt_pk_fp8_f32 v10, v20, v21 op_sel:[0,0,1]
	v_cvt_pk_fp8_f32 v12, v28, v29 op_sel:[0,0,1]
	v_cvt_pk_fp8_f32 v11, v22, v23
	v_cvt_pk_fp8_f32 v13, v30, v31
	v_cvt_pk_fp8_f32 v11, v24, v25 op_sel:[0,0,1]
	v_cvt_pk_fp8_f32 v13, v32, v33 op_sel:[0,0,1]
	s_nop 0
	global_store_dwordx2 v[6:7], v[10:11], off
	global_store_dwordx2 v[46:47], v[12:13], off
	v_add_u32_e32 v9, 32, v8
	v_mad_i64_i32 v[6:7], s[6:7], v9, s8, v[4:5]
	v_add_u32_e32 v9, 48, v8
	v_mad_i64_i32 v[46:47], s[6:7], v9, s8, v[4:5]
	v_pk_mul_f32 v[18:19], v[158:159], s[100:101] op_sel_hi:[1,0]
	v_pk_mul_f32 v[20:21], v[160:161], s[100:101] op_sel_hi:[1,0]
	v_pk_mul_f32 v[22:23], v[150:151], s[100:101] op_sel_hi:[1,0]
	v_pk_mul_f32 v[24:25], v[152:153], s[100:101] op_sel_hi:[1,0]
	v_pk_mul_f32 v[26:27], v[142:143], s[100:101] op_sel_hi:[1,0]
	v_pk_mul_f32 v[28:29], v[144:145], s[100:101] op_sel_hi:[1,0]
	v_pk_mul_f32 v[30:31], v[134:135], s[100:101] op_sel_hi:[1,0]
	v_pk_mul_f32 v[32:33], v[136:137], s[100:101] op_sel_hi:[1,0]
	v_lshl_add_u64 v[6:7], v[6:7], 0, v[2:3]
	v_lshl_add_u64 v[46:47], v[46:47], 0, v[2:3]
	v_exp_f32_e32 v18, v18
	v_exp_f32_e32 v19, v19
	v_exp_f32_e32 v20, v20
	v_exp_f32_e32 v21, v21
	v_exp_f32_e32 v22, v22
	v_exp_f32_e32 v23, v23
	v_exp_f32_e32 v24, v24
	v_exp_f32_e32 v25, v25
	v_exp_f32_e32 v26, v26
	v_exp_f32_e32 v27, v27
	v_exp_f32_e32 v28, v28
	v_exp_f32_e32 v29, v29
	v_exp_f32_e32 v30, v30
	v_exp_f32_e32 v31, v31
	v_exp_f32_e32 v32, v32
	v_exp_f32_e32 v33, v33
	v_pk_add_f32 v[18:19], v[18:19], 1.0 op_sel_hi:[1,0]
	v_pk_add_f32 v[20:21], v[20:21], 1.0 op_sel_hi:[1,0]
	v_pk_add_f32 v[22:23], v[22:23], 1.0 op_sel_hi:[1,0]
	v_pk_add_f32 v[24:25], v[24:25], 1.0 op_sel_hi:[1,0]
	v_pk_add_f32 v[26:27], v[26:27], 1.0 op_sel_hi:[1,0]
	v_pk_add_f32 v[28:29], v[28:29], 1.0 op_sel_hi:[1,0]
	v_pk_add_f32 v[30:31], v[30:31], 1.0 op_sel_hi:[1,0]
	v_pk_add_f32 v[32:33], v[32:33], 1.0 op_sel_hi:[1,0]
	v_rcp_f32_e32 v18, v18
	v_rcp_f32_e32 v19, v19
	v_rcp_f32_e32 v20, v20
	v_rcp_f32_e32 v21, v21
	v_rcp_f32_e32 v22, v22
	v_rcp_f32_e32 v23, v23
	v_rcp_f32_e32 v24, v24
	v_rcp_f32_e32 v25, v25
	v_rcp_f32_e32 v26, v26
	v_rcp_f32_e32 v27, v27
	v_rcp_f32_e32 v28, v28
	v_rcp_f32_e32 v29, v29
	v_rcp_f32_e32 v30, v30
	v_rcp_f32_e32 v31, v31
	v_rcp_f32_e32 v32, v32
	v_rcp_f32_e32 v33, v33
	v_pk_mul_f32 v[18:19], v[158:159], v[18:19]
	v_pk_mul_f32 v[20:21], v[160:161], v[20:21]
	v_pk_mul_f32 v[22:23], v[150:151], v[22:23]
	v_pk_mul_f32 v[24:25], v[152:153], v[24:25]
	v_pk_mul_f32 v[26:27], v[142:143], v[26:27]
	v_pk_mul_f32 v[28:29], v[144:145], v[28:29]
	v_pk_mul_f32 v[30:31], v[134:135], v[30:31]
	v_pk_mul_f32 v[32:33], v[136:137], v[32:33]
	v_pk_mul_f32 v[18:19], v[18:19], v[154:155]
	v_pk_mul_f32 v[20:21], v[20:21], v[156:157]
	v_pk_mul_f32 v[22:23], v[22:23], v[146:147]
	v_pk_mul_f32 v[24:25], v[24:25], v[148:149]
	v_pk_mul_f32 v[26:27], v[26:27], v[138:139]
	v_pk_mul_f32 v[28:29], v[28:29], v[140:141]
	v_pk_mul_f32 v[30:31], v[30:31], v[130:131]
	v_pk_mul_f32 v[32:33], v[32:33], v[132:133]
	v_pk_mul_f32 v[18:19], v[18:19], s[100:101] op_sel:[0,1] op_sel_hi:[1,1]
	v_pk_mul_f32 v[20:21], v[20:21], s[100:101] op_sel:[0,1] op_sel_hi:[1,1]
	v_pk_mul_f32 v[22:23], v[22:23], s[100:101] op_sel:[0,1] op_sel_hi:[1,1]
	v_pk_mul_f32 v[24:25], v[24:25], s[100:101] op_sel:[0,1] op_sel_hi:[1,1]
	v_pk_mul_f32 v[26:27], v[26:27], s[100:101] op_sel:[0,1] op_sel_hi:[1,1]
	v_pk_mul_f32 v[28:29], v[28:29], s[100:101] op_sel:[0,1] op_sel_hi:[1,1]
	v_pk_mul_f32 v[30:31], v[30:31], s[100:101] op_sel:[0,1] op_sel_hi:[1,1]
	v_pk_mul_f32 v[32:33], v[32:33], s[100:101] op_sel:[0,1] op_sel_hi:[1,1]
	v_cvt_pk_fp8_f32 v10, v18, v19
	v_cvt_pk_fp8_f32 v12, v26, v27
	v_cvt_pk_fp8_f32 v10, v20, v21 op_sel:[0,0,1]
	v_cvt_pk_fp8_f32 v12, v28, v29 op_sel:[0,0,1]
	v_cvt_pk_fp8_f32 v11, v22, v23
	v_cvt_pk_fp8_f32 v13, v30, v31
	v_cvt_pk_fp8_f32 v11, v24, v25 op_sel:[0,0,1]
	v_cvt_pk_fp8_f32 v13, v32, v33 op_sel:[0,0,1]
	s_nop 0
	global_store_dwordx2 v[6:7], v[10:11], off
	global_store_dwordx2 v[46:47], v[12:13], off
	v_add_u32_e32 v9, 0x80, v8
	v_mad_i64_i32 v[6:7], s[6:7], v9, s8, v[4:5]
	v_add_u32_e32 v9, 0x90, v8
	v_mad_i64_i32 v[46:47], s[6:7], v9, s8, v[4:5]
	v_pk_mul_f32 v[18:19], v[126:127], s[100:101] op_sel_hi:[1,0]
	v_pk_mul_f32 v[20:21], v[128:129], s[100:101] op_sel_hi:[1,0]
	v_pk_mul_f32 v[22:23], v[118:119], s[100:101] op_sel_hi:[1,0]
	v_pk_mul_f32 v[24:25], v[120:121], s[100:101] op_sel_hi:[1,0]
	v_pk_mul_f32 v[26:27], v[110:111], s[100:101] op_sel_hi:[1,0]
	v_pk_mul_f32 v[28:29], v[112:113], s[100:101] op_sel_hi:[1,0]
	v_pk_mul_f32 v[30:31], v[102:103], s[100:101] op_sel_hi:[1,0]
	v_pk_mul_f32 v[32:33], v[104:105], s[100:101] op_sel_hi:[1,0]
	v_lshl_add_u64 v[6:7], v[6:7], 0, v[2:3]
	v_lshl_add_u64 v[46:47], v[46:47], 0, v[2:3]
	v_exp_f32_e32 v18, v18
	v_exp_f32_e32 v19, v19
	v_exp_f32_e32 v20, v20
	v_exp_f32_e32 v21, v21
	v_exp_f32_e32 v22, v22
	v_exp_f32_e32 v23, v23
	v_exp_f32_e32 v24, v24
	v_exp_f32_e32 v25, v25
	v_exp_f32_e32 v26, v26
	v_exp_f32_e32 v27, v27
	v_exp_f32_e32 v28, v28
	v_exp_f32_e32 v29, v29
	v_exp_f32_e32 v30, v30
	v_exp_f32_e32 v31, v31
	v_exp_f32_e32 v32, v32
	v_exp_f32_e32 v33, v33
	v_pk_add_f32 v[18:19], v[18:19], 1.0 op_sel_hi:[1,0]
	v_pk_add_f32 v[20:21], v[20:21], 1.0 op_sel_hi:[1,0]
	v_pk_add_f32 v[22:23], v[22:23], 1.0 op_sel_hi:[1,0]
	v_pk_add_f32 v[24:25], v[24:25], 1.0 op_sel_hi:[1,0]
	v_pk_add_f32 v[26:27], v[26:27], 1.0 op_sel_hi:[1,0]
	v_pk_add_f32 v[28:29], v[28:29], 1.0 op_sel_hi:[1,0]
	v_pk_add_f32 v[30:31], v[30:31], 1.0 op_sel_hi:[1,0]
	v_pk_add_f32 v[32:33], v[32:33], 1.0 op_sel_hi:[1,0]
	v_rcp_f32_e32 v18, v18
	v_rcp_f32_e32 v19, v19
	v_rcp_f32_e32 v20, v20
	v_rcp_f32_e32 v21, v21
	v_rcp_f32_e32 v22, v22
	v_rcp_f32_e32 v23, v23
	v_rcp_f32_e32 v24, v24
	v_rcp_f32_e32 v25, v25
	v_rcp_f32_e32 v26, v26
	v_rcp_f32_e32 v27, v27
	v_rcp_f32_e32 v28, v28
	v_rcp_f32_e32 v29, v29
	v_rcp_f32_e32 v30, v30
	v_rcp_f32_e32 v31, v31
	v_rcp_f32_e32 v32, v32
	v_rcp_f32_e32 v33, v33
	v_pk_mul_f32 v[18:19], v[126:127], v[18:19]
	v_pk_mul_f32 v[20:21], v[128:129], v[20:21]
	v_pk_mul_f32 v[22:23], v[118:119], v[22:23]
	v_pk_mul_f32 v[24:25], v[120:121], v[24:25]
	v_pk_mul_f32 v[26:27], v[110:111], v[26:27]
	v_pk_mul_f32 v[28:29], v[112:113], v[28:29]
	v_pk_mul_f32 v[30:31], v[102:103], v[30:31]
	v_pk_mul_f32 v[32:33], v[104:105], v[32:33]
	v_pk_mul_f32 v[18:19], v[18:19], v[122:123]
	v_pk_mul_f32 v[20:21], v[20:21], v[124:125]
	v_pk_mul_f32 v[22:23], v[22:23], v[114:115]
	v_pk_mul_f32 v[24:25], v[24:25], v[116:117]
	v_pk_mul_f32 v[26:27], v[26:27], v[106:107]
	v_pk_mul_f32 v[28:29], v[28:29], v[108:109]
	v_pk_mul_f32 v[30:31], v[30:31], v[98:99]
	v_pk_mul_f32 v[32:33], v[32:33], v[100:101]
	v_pk_mul_f32 v[18:19], v[18:19], s[100:101] op_sel:[0,1] op_sel_hi:[1,1]
	v_pk_mul_f32 v[20:21], v[20:21], s[100:101] op_sel:[0,1] op_sel_hi:[1,1]
	v_pk_mul_f32 v[22:23], v[22:23], s[100:101] op_sel:[0,1] op_sel_hi:[1,1]
	v_pk_mul_f32 v[24:25], v[24:25], s[100:101] op_sel:[0,1] op_sel_hi:[1,1]
	v_pk_mul_f32 v[26:27], v[26:27], s[100:101] op_sel:[0,1] op_sel_hi:[1,1]
	v_pk_mul_f32 v[28:29], v[28:29], s[100:101] op_sel:[0,1] op_sel_hi:[1,1]
	v_pk_mul_f32 v[30:31], v[30:31], s[100:101] op_sel:[0,1] op_sel_hi:[1,1]
	v_pk_mul_f32 v[32:33], v[32:33], s[100:101] op_sel:[0,1] op_sel_hi:[1,1]
	v_cvt_pk_fp8_f32 v10, v18, v19
	v_cvt_pk_fp8_f32 v12, v26, v27
	v_cvt_pk_fp8_f32 v10, v20, v21 op_sel:[0,0,1]
	v_cvt_pk_fp8_f32 v12, v28, v29 op_sel:[0,0,1]
	v_cvt_pk_fp8_f32 v11, v22, v23
	v_cvt_pk_fp8_f32 v13, v30, v31
	v_cvt_pk_fp8_f32 v11, v24, v25 op_sel:[0,0,1]
	v_cvt_pk_fp8_f32 v13, v32, v33 op_sel:[0,0,1]
	s_nop 0
	global_store_dwordx2 v[6:7], v[10:11], off
	global_store_dwordx2 v[46:47], v[12:13], off
	v_add_u32_e32 v9, 0xa0, v8
	v_mad_i64_i32 v[6:7], s[6:7], v9, s8, v[4:5]
	v_add_u32_e32 v9, 0xb0, v8
	v_mad_i64_i32 v[46:47], s[6:7], v9, s8, v[4:5]
	v_pk_mul_f32 v[18:19], v[94:95], s[100:101] op_sel_hi:[1,0]
	v_pk_mul_f32 v[20:21], v[96:97], s[100:101] op_sel_hi:[1,0]
	v_pk_mul_f32 v[22:23], v[86:87], s[100:101] op_sel_hi:[1,0]
	v_pk_mul_f32 v[24:25], v[88:89], s[100:101] op_sel_hi:[1,0]
	v_pk_mul_f32 v[26:27], v[78:79], s[100:101] op_sel_hi:[1,0]
	v_pk_mul_f32 v[28:29], v[80:81], s[100:101] op_sel_hi:[1,0]
	v_pk_mul_f32 v[30:31], v[70:71], s[100:101] op_sel_hi:[1,0]
	v_pk_mul_f32 v[32:33], v[72:73], s[100:101] op_sel_hi:[1,0]
	v_lshl_add_u64 v[6:7], v[6:7], 0, v[2:3]
	v_lshl_add_u64 v[46:47], v[46:47], 0, v[2:3]
	v_exp_f32_e32 v18, v18
	v_exp_f32_e32 v19, v19
	v_exp_f32_e32 v20, v20
	v_exp_f32_e32 v21, v21
	v_exp_f32_e32 v22, v22
	v_exp_f32_e32 v23, v23
	v_exp_f32_e32 v24, v24
	v_exp_f32_e32 v25, v25
	v_exp_f32_e32 v26, v26
	v_exp_f32_e32 v27, v27
	v_exp_f32_e32 v28, v28
	v_exp_f32_e32 v29, v29
	v_exp_f32_e32 v30, v30
	v_exp_f32_e32 v31, v31
	v_exp_f32_e32 v32, v32
	v_exp_f32_e32 v33, v33
	v_pk_add_f32 v[18:19], v[18:19], 1.0 op_sel_hi:[1,0]
	v_pk_add_f32 v[20:21], v[20:21], 1.0 op_sel_hi:[1,0]
	v_pk_add_f32 v[22:23], v[22:23], 1.0 op_sel_hi:[1,0]
	v_pk_add_f32 v[24:25], v[24:25], 1.0 op_sel_hi:[1,0]
	v_pk_add_f32 v[26:27], v[26:27], 1.0 op_sel_hi:[1,0]
	v_pk_add_f32 v[28:29], v[28:29], 1.0 op_sel_hi:[1,0]
	v_pk_add_f32 v[30:31], v[30:31], 1.0 op_sel_hi:[1,0]
	v_pk_add_f32 v[32:33], v[32:33], 1.0 op_sel_hi:[1,0]
	v_rcp_f32_e32 v18, v18
	v_rcp_f32_e32 v19, v19
	v_rcp_f32_e32 v20, v20
	v_rcp_f32_e32 v21, v21
	v_rcp_f32_e32 v22, v22
	v_rcp_f32_e32 v23, v23
	v_rcp_f32_e32 v24, v24
	v_rcp_f32_e32 v25, v25
	v_rcp_f32_e32 v26, v26
	v_rcp_f32_e32 v27, v27
	v_rcp_f32_e32 v28, v28
	v_rcp_f32_e32 v29, v29
	v_rcp_f32_e32 v30, v30
	v_rcp_f32_e32 v31, v31
	v_rcp_f32_e32 v32, v32
	v_rcp_f32_e32 v33, v33
	v_pk_mul_f32 v[18:19], v[94:95], v[18:19]
	v_pk_mul_f32 v[20:21], v[96:97], v[20:21]
	v_pk_mul_f32 v[22:23], v[86:87], v[22:23]
	v_pk_mul_f32 v[24:25], v[88:89], v[24:25]
	v_pk_mul_f32 v[26:27], v[78:79], v[26:27]
	v_pk_mul_f32 v[28:29], v[80:81], v[28:29]
	v_pk_mul_f32 v[30:31], v[70:71], v[30:31]
	v_pk_mul_f32 v[32:33], v[72:73], v[32:33]
	v_pk_mul_f32 v[18:19], v[18:19], v[90:91]
	v_pk_mul_f32 v[20:21], v[20:21], v[92:93]
	v_pk_mul_f32 v[22:23], v[22:23], v[82:83]
	v_pk_mul_f32 v[24:25], v[24:25], v[84:85]
	v_pk_mul_f32 v[26:27], v[26:27], v[74:75]
	v_pk_mul_f32 v[28:29], v[28:29], v[76:77]
	v_pk_mul_f32 v[30:31], v[30:31], v[66:67]
	v_pk_mul_f32 v[32:33], v[32:33], v[68:69]
	v_pk_mul_f32 v[18:19], v[18:19], s[100:101] op_sel:[0,1] op_sel_hi:[1,1]
	v_pk_mul_f32 v[20:21], v[20:21], s[100:101] op_sel:[0,1] op_sel_hi:[1,1]
	v_pk_mul_f32 v[22:23], v[22:23], s[100:101] op_sel:[0,1] op_sel_hi:[1,1]
	v_pk_mul_f32 v[24:25], v[24:25], s[100:101] op_sel:[0,1] op_sel_hi:[1,1]
	v_pk_mul_f32 v[26:27], v[26:27], s[100:101] op_sel:[0,1] op_sel_hi:[1,1]
	v_pk_mul_f32 v[28:29], v[28:29], s[100:101] op_sel:[0,1] op_sel_hi:[1,1]
	v_pk_mul_f32 v[30:31], v[30:31], s[100:101] op_sel:[0,1] op_sel_hi:[1,1]
	v_pk_mul_f32 v[32:33], v[32:33], s[100:101] op_sel:[0,1] op_sel_hi:[1,1]
	v_cvt_pk_fp8_f32 v10, v18, v19
	v_cvt_pk_fp8_f32 v12, v26, v27
	v_cvt_pk_fp8_f32 v10, v20, v21 op_sel:[0,0,1]
	v_cvt_pk_fp8_f32 v12, v28, v29 op_sel:[0,0,1]
	v_cvt_pk_fp8_f32 v11, v22, v23
	v_cvt_pk_fp8_f32 v13, v30, v31
	v_cvt_pk_fp8_f32 v11, v24, v25 op_sel:[0,0,1]
	v_cvt_pk_fp8_f32 v13, v32, v33 op_sel:[0,0,1]
	s_nop 0
	global_store_dwordx2 v[6:7], v[10:11], off
	global_store_dwordx2 v[46:47], v[12:13], off
	s_cbranch_vccnz .LBB0_1010

.LBB0_1004:
	s_xor_b64 s[58:59], s[6:7], -1
	s_add_u32 s56, s60, s42
	s_addc_u32 s57, s61, s43
	s_and_b64 s[8:9], s[6:7], exec
	s_cselect_b32 s14, s57, s27
	s_cselect_b32 s16, s56, s26
	s_add_u32 s17, s26, 0x100
	v_mov_b32_e32 v66, 0
	s_addc_u32 s18, s27, 0
	s_mov_b32 s19, -2
	s_mov_b64 s[26:27], s[28:29]
	v_mov_b32_e32 v67, v66
	v_mov_b64_e32 v[68:69], 0
	v_mov_b64_e32 v[70:71], 0
	v_mov_b64_e32 v[72:73], 0
	v_mov_b64_e32 v[74:75], 0
	v_mov_b64_e32 v[76:77], 0
	v_mov_b64_e32 v[78:79], 0
	v_mov_b64_e32 v[80:81], 0
	v_mov_b64_e32 v[82:83], 0
	v_mov_b64_e32 v[84:85], 0
	v_mov_b64_e32 v[86:87], 0
	v_mov_b64_e32 v[88:89], 0
	v_mov_b64_e32 v[90:91], 0
	v_mov_b64_e32 v[92:93], 0
	v_mov_b64_e32 v[94:95], 0
	v_mov_b64_e32 v[96:97], 0
	v_mov_b64_e32 v[98:99], 0
	v_mov_b64_e32 v[100:101], 0
	v_mov_b64_e32 v[102:103], 0
	v_mov_b64_e32 v[104:105], 0
	v_mov_b64_e32 v[106:107], 0
	v_mov_b64_e32 v[108:109], 0
	v_mov_b64_e32 v[110:111], 0
	v_mov_b64_e32 v[112:113], 0
	v_mov_b64_e32 v[114:115], 0
	v_mov_b64_e32 v[116:117], 0
	v_mov_b64_e32 v[118:119], 0
	v_mov_b64_e32 v[120:121], 0
	v_mov_b64_e32 v[122:123], 0
	v_mov_b64_e32 v[124:125], 0
	v_mov_b64_e32 v[126:127], 0
	v_mov_b64_e32 v[128:129], 0
	v_mov_b64_e32 v[130:131], 0
	v_mov_b64_e32 v[132:133], 0
	v_mov_b64_e32 v[134:135], 0
	v_mov_b64_e32 v[136:137], 0
	v_mov_b64_e32 v[138:139], 0
	v_mov_b64_e32 v[140:141], 0
	v_mov_b64_e32 v[142:143], 0
	v_mov_b64_e32 v[144:145], 0
	v_mov_b64_e32 v[146:147], 0
	v_mov_b64_e32 v[148:149], 0
	v_mov_b64_e32 v[150:151], 0
	v_mov_b64_e32 v[152:153], 0
	v_mov_b64_e32 v[154:155], 0
	v_mov_b64_e32 v[156:157], 0
	v_mov_b64_e32 v[158:159], 0
	v_mov_b64_e32 v[160:161], 0
	v_mov_b64_e32 v[162:163], 0
	v_mov_b64_e32 v[164:165], 0
	v_mov_b64_e32 v[166:167], 0
	v_mov_b64_e32 v[168:169], 0
	v_mov_b64_e32 v[170:171], 0
	v_mov_b64_e32 v[172:173], 0
	v_mov_b64_e32 v[174:175], 0
	v_mov_b64_e32 v[176:177], 0
	v_mov_b64_e32 v[178:179], 0
	v_mov_b64_e32 v[180:181], 0
	v_mov_b64_e32 v[182:183], 0
	v_mov_b64_e32 v[184:185], 0
	v_mov_b64_e32 v[186:187], 0
	v_mov_b64_e32 v[188:189], 0
	v_mov_b64_e32 v[190:191], 0
	v_mov_b64_e32 v[192:193], 0
	s_branch .LBB0_1007

.LBB0_1192:
	s_xor_b64 s[38:39], s[8:9], -1
	v_readfirstlane_b32 s26, v2
	v_readfirstlane_b32 s27, v3
	s_add_u32 s40, s10, s26
	s_addc_u32 s41, s13, s27
	v_readfirstlane_b32 s36, v4
	s_and_b64 s[42:43], s[8:9], exec
	v_readfirstlane_b32 s37, v5
	s_cselect_b32 s57, s41, s45
	s_cselect_b32 s58, s40, s44
	s_add_u32 s42, s14, s36
	s_addc_u32 s43, s16, s37
	s_and_b64 s[8:9], s[8:9], exec
	s_cselect_b32 s8, s43, s47
	s_cselect_b32 s9, s42, s46
	s_add_u32 s44, s44, 0x30080
	s_addc_u32 s45, s45, 0
	s_add_u32 s59, s46, 0x100
	v_mov_b32_e32 v34, 0
	s_addc_u32 s60, s47, 0
	s_mov_b32 s61, -2
	v_mov_b32_e32 v35, v34
	v_mov_b64_e32 v[36:37], 0
	v_mov_b64_e32 v[38:39], 0
	v_mov_b64_e32 v[40:41], 0
	v_mov_b64_e32 v[42:43], 0
	v_mov_b64_e32 v[44:45], 0
	v_mov_b64_e32 v[46:47], 0
	v_mov_b64_e32 v[48:49], 0
	v_mov_b64_e32 v[50:51], 0
	v_mov_b64_e32 v[52:53], 0
	v_mov_b64_e32 v[54:55], 0
	v_mov_b64_e32 v[56:57], 0
	v_mov_b64_e32 v[58:59], 0
	v_mov_b64_e32 v[60:61], 0
	v_mov_b64_e32 v[62:63], 0
	v_mov_b64_e32 v[64:65], 0
	v_mov_b64_e32 v[66:67], 0
	v_mov_b64_e32 v[68:69], 0
	v_mov_b64_e32 v[70:71], 0
	v_mov_b64_e32 v[72:73], 0
	v_mov_b64_e32 v[74:75], 0
	v_mov_b64_e32 v[76:77], 0
	v_mov_b64_e32 v[78:79], 0
	v_mov_b64_e32 v[80:81], 0
	v_mov_b64_e32 v[82:83], 0
	v_mov_b64_e32 v[84:85], 0
	v_mov_b64_e32 v[86:87], 0
	v_mov_b64_e32 v[88:89], 0
	v_mov_b64_e32 v[90:91], 0
	v_mov_b64_e32 v[92:93], 0
	v_mov_b64_e32 v[94:95], 0
	v_mov_b64_e32 v[96:97], 0
	v_mov_b64_e32 v[98:99], 0
	v_mov_b64_e32 v[100:101], 0
	v_mov_b64_e32 v[102:103], 0
	v_mov_b64_e32 v[104:105], 0
	v_mov_b64_e32 v[106:107], 0
	v_mov_b64_e32 v[108:109], 0
	v_mov_b64_e32 v[110:111], 0
	v_mov_b64_e32 v[112:113], 0
	v_mov_b64_e32 v[114:115], 0
	v_mov_b64_e32 v[116:117], 0
	v_mov_b64_e32 v[118:119], 0
	v_mov_b64_e32 v[120:121], 0
	v_mov_b64_e32 v[122:123], 0
	v_mov_b64_e32 v[124:125], 0
	v_mov_b64_e32 v[126:127], 0
	v_mov_b64_e32 v[128:129], 0
	v_mov_b64_e32 v[130:131], 0
	v_mov_b64_e32 v[132:133], 0
	v_mov_b64_e32 v[134:135], 0
	v_mov_b64_e32 v[136:137], 0
	v_mov_b64_e32 v[138:139], 0
	v_mov_b64_e32 v[140:141], 0
	v_mov_b64_e32 v[142:143], 0
	v_mov_b64_e32 v[144:145], 0
	v_mov_b64_e32 v[146:147], 0
	v_mov_b64_e32 v[148:149], 0
	v_mov_b64_e32 v[150:151], 0
	v_mov_b64_e32 v[152:153], 0
	v_mov_b64_e32 v[154:155], 0
	v_mov_b64_e32 v[156:157], 0
	v_mov_b64_e32 v[158:159], 0
	v_mov_b64_e32 v[160:161], 0
